# v45
# speedup vs baseline: 1.0061x; 1.0009x over previous
.LBB0_21:
	s_setprio 2
	s_and_b64 vcc, exec, s[4:5]
	s_cbranch_vccz .LBB0_71
	s_load_dwordx4 s[4:7], s[0:1], 0x8
	s_movk_i32 s3, 0x200
	v_cmp_gt_u32_e32 vcc, s3, v0
	v_lshlrev_b32_e32 v19, 2, v0
	s_and_saveexec_b64 s[8:9], vcc
	v_mov_b32_e32 v1, 0
	ds_write_b32 v19, v1 offset:25024
	s_or_b64 exec, exec, s[8:9]
	s_mul_i32 s10, s2, 0x1870
	s_mov_b32 s11, 0
	s_lshl_b64 s[24:25], s[10:11], 2
	s_waitcnt lgkmcnt(0)
	s_add_u32 s6, s6, s24
	s_addc_u32 s7, s7, s25
	s_add_u32 s8, s4, s24
	v_lshlrev_b32_e32 v18, 4, v0
	s_barrier
	s_addc_u32 s9, s5, s25
	global_load_dwordx4 v[14:17], v18, s[6:7]
	global_load_dwordx4 v[10:13], v18, s[8:9]
	v_mov_b32_e32 v1, 0x185190
	v_sub_u32_e64 v1, s10, v1 clamp
	v_sub_u32_e32 v1, 0x1870, v1
	v_lshrrev_b32_e32 v1, 2, v1
	v_or_b32_e32 v21, 0x400, v0
	v_mov_b32_e32 v20, 0
	v_cmp_lt_u32_e64 s[4:5], v21, v1
	v_mov_b32_e32 v2, -1
	v_mov_b32_e32 v6, 0
	v_mov_b32_e32 v7, 0
	v_mov_b32_e32 v8, 0
	v_mov_b32_e32 v9, 0
	v_mov_b32_e32 v3, -1
	v_mov_b32_e32 v4, -1
	v_mov_b32_e32 v5, -1
	s_and_saveexec_b64 s[10:11], s[4:5]
	s_cbranch_execz .LBB0_26
	v_lshlrev_b32_e32 v21, 4, v21
	global_load_dwordx4 v[2:5], v21, s[6:7]
	global_load_dwordx4 v[6:9], v21, s[8:9]
